# v10 + cv_run weight-conversion double buffering restored: join-point waits vmcnt(15..0) no longer drain the next batch (vmcnt(31..16) + explicit waits on the no-issue edges, vmcnt(20) before batch B)
# baseline (speedup 1.0000x reference)
.LBB0_531:
	s_waitcnt vmcnt(31)
	v_mov_b32_e32 v130, v2
	s_waitcnt vmcnt(30)
	v_mov_b32_e32 v131, v6
	v_pk_mul_f32 v[130:131], v[130:131], s[72:73] op_sel_hi:[1,0]
	v_mov_b32_e32 v0, v1
	v_cvt_pk_fp8_f32 v0, v130, v131
	s_waitcnt vmcnt(29)
	v_mov_b32_e32 v130, v10
	s_waitcnt vmcnt(28)
	v_mov_b32_e32 v131, v14
	v_pk_mul_f32 v[130:131], v[130:131], s[72:73] op_sel_hi:[1,0]
	v_mov_b32_e32 v132, v1
	v_cvt_pk_fp8_f32 v0, v130, v131 op_sel:[0,0,1]
	v_mov_b32_e32 v130, v3
	v_mov_b32_e32 v131, v7
	v_pk_mul_f32 v[130:131], v[130:131], s[72:73] op_sel_hi:[1,0]
	v_mov_b32_e32 v133, v1
	v_cvt_pk_fp8_f32 v132, v130, v131
	v_mov_b32_e32 v130, v11
	v_mov_b32_e32 v131, v15
	v_pk_mul_f32 v[130:131], v[130:131], s[72:73] op_sel_hi:[1,0]
	v_mov_b32_e32 v138, v1
	v_cvt_pk_fp8_f32 v132, v130, v131 op_sel:[0,0,1]
	v_mov_b32_e32 v130, v4
	v_mov_b32_e32 v131, v8
	v_pk_mul_f32 v[130:131], v[130:131], s[72:73] op_sel_hi:[1,0]
	v_mov_b32_e32 v139, v1
	v_cvt_pk_fp8_f32 v133, v130, v131
	v_mov_b32_e32 v130, v12
	v_mov_b32_e32 v131, v16
	v_pk_mul_f32 v[130:131], v[130:131], s[72:73] op_sel_hi:[1,0]
	v_mov_b32_e32 v146, v1
	v_cvt_pk_fp8_f32 v133, v130, v131 op_sel:[0,0,1]
	v_mov_b32_e32 v130, v5
	v_mov_b32_e32 v131, v9
	v_pk_mul_f32 v[130:131], v[130:131], s[72:73] op_sel_hi:[1,0]
	v_add_u32_e32 v145, 0x4000, v143
	v_cvt_pk_fp8_f32 v138, v130, v131
	v_mov_b32_e32 v130, v13
	v_mov_b32_e32 v131, v17
	v_pk_mul_f32 v[130:131], v[130:131], s[72:73] op_sel_hi:[1,0]
	v_add_u32_e32 v144, 0x8400, v143
	v_cvt_pk_fp8_f32 v138, v130, v131 op_sel:[0,0,1]
	s_waitcnt vmcnt(27)
	v_mov_b32_e32 v130, v18
	s_waitcnt vmcnt(26)
	v_mov_b32_e32 v131, v22
	ds_write2_b32 v143, v0, v132 offset1:33
	ds_write2_b32 v143, v133, v138 offset0:66 offset1:99
	v_pk_mul_f32 v[130:131], v[130:131], s[72:73] op_sel_hi:[1,0]
	v_mov_b32_e32 v0, v1
	v_cvt_pk_fp8_f32 v0, v130, v131
	s_waitcnt vmcnt(25)
	v_mov_b32_e32 v130, v26
	s_waitcnt vmcnt(24)
	v_mov_b32_e32 v131, v30
	v_pk_mul_f32 v[130:131], v[130:131], s[72:73] op_sel_hi:[1,0]
	v_mov_b32_e32 v132, v1
	v_cvt_pk_fp8_f32 v0, v130, v131 op_sel:[0,0,1]
	v_mov_b32_e32 v130, v19
	v_mov_b32_e32 v131, v23
	v_pk_mul_f32 v[130:131], v[130:131], s[72:73] op_sel_hi:[1,0]
	v_mov_b32_e32 v133, v1
	v_cvt_pk_fp8_f32 v132, v130, v131
	v_mov_b32_e32 v130, v27
	v_mov_b32_e32 v131, v31
	v_pk_mul_f32 v[130:131], v[130:131], s[72:73] op_sel_hi:[1,0]
	v_mov_b32_e32 v138, v1
	v_cvt_pk_fp8_f32 v132, v130, v131 op_sel:[0,0,1]
	v_mov_b32_e32 v130, v20
	v_mov_b32_e32 v131, v24
	v_pk_mul_f32 v[130:131], v[130:131], s[72:73] op_sel_hi:[1,0]
	v_mov_b32_e32 v147, v1
	v_cvt_pk_fp8_f32 v133, v130, v131
	v_mov_b32_e32 v130, v28
	v_mov_b32_e32 v131, v32
	v_pk_mul_f32 v[130:131], v[130:131], s[72:73] op_sel_hi:[1,0]
	s_cmp_lt_i32 s40, 2
	v_cvt_pk_fp8_f32 v133, v130, v131 op_sel:[0,0,1]
	v_mov_b32_e32 v130, v21
	v_mov_b32_e32 v131, v25
	v_pk_mul_f32 v[130:131], v[130:131], s[72:73] op_sel_hi:[1,0]
	s_nop 0
	v_cvt_pk_fp8_f32 v138, v130, v131
	v_mov_b32_e32 v130, v29
	v_mov_b32_e32 v131, v33
	v_pk_mul_f32 v[130:131], v[130:131], s[72:73] op_sel_hi:[1,0]
	s_nop 0
	v_cvt_pk_fp8_f32 v138, v130, v131 op_sel:[0,0,1]
	s_waitcnt vmcnt(23)
	v_mov_b32_e32 v130, v50
	s_waitcnt vmcnt(22)
	v_mov_b32_e32 v131, v54
	v_pk_mul_f32 v[130:131], v[130:131], s[72:73] op_sel_hi:[1,0]
	ds_write2_b32 v145, v0, v132 offset0:128 offset1:161
	ds_write2_b32 v145, v133, v138 offset0:194 offset1:227
	v_cvt_pk_fp8_f32 v139, v130, v131
	s_waitcnt vmcnt(21)
	v_mov_b32_e32 v130, v58
	s_waitcnt vmcnt(20)
	v_mov_b32_e32 v131, v62
	v_pk_mul_f32 v[130:131], v[130:131], s[72:73] op_sel_hi:[1,0]
	v_mov_b32_e32 v0, v1
	v_cvt_pk_fp8_f32 v139, v130, v131 op_sel:[0,0,1]
	v_mov_b32_e32 v130, v51
	v_mov_b32_e32 v131, v55
	v_pk_mul_f32 v[130:131], v[130:131], s[72:73] op_sel_hi:[1,0]
	v_mov_b32_e32 v132, v1
	v_cvt_pk_fp8_f32 v146, v130, v131
	v_mov_b32_e32 v130, v59
	v_mov_b32_e32 v131, v63
	v_pk_mul_f32 v[130:131], v[130:131], s[72:73] op_sel_hi:[1,0]
	v_mov_b32_e32 v133, v1
	v_cvt_pk_fp8_f32 v146, v130, v131 op_sel:[0,0,1]
	v_mov_b32_e32 v130, v52
	v_mov_b32_e32 v131, v56
	v_pk_mul_f32 v[130:131], v[130:131], s[72:73] op_sel_hi:[1,0]
	v_mov_b32_e32 v138, v1
	v_cvt_pk_fp8_f32 v0, v130, v131
	v_mov_b32_e32 v130, v60
	v_mov_b32_e32 v131, v64
	v_pk_mul_f32 v[130:131], v[130:131], s[72:73] op_sel_hi:[1,0]
	ds_write2_b32 v144, v139, v146 offset1:33
	v_cvt_pk_fp8_f32 v0, v130, v131 op_sel:[0,0,1]
	v_mov_b32_e32 v130, v53
	v_mov_b32_e32 v131, v57
	v_pk_mul_f32 v[130:131], v[130:131], s[72:73] op_sel_hi:[1,0]
	v_mov_b32_e32 v139, v1
	v_cvt_pk_fp8_f32 v132, v130, v131
	v_mov_b32_e32 v130, v61
	v_mov_b32_e32 v131, v65
	v_pk_mul_f32 v[130:131], v[130:131], s[72:73] op_sel_hi:[1,0]
	v_add_u32_e32 v146, 0xc400, v143
	v_cvt_pk_fp8_f32 v132, v130, v131 op_sel:[0,0,1]
	s_waitcnt vmcnt(19)
	v_mov_b32_e32 v130, v82
	s_waitcnt vmcnt(18)
	v_mov_b32_e32 v131, v86
	v_pk_mul_f32 v[130:131], v[130:131], s[72:73] op_sel_hi:[1,0]
	ds_write2_b32 v144, v0, v132 offset0:66 offset1:99
	v_cvt_pk_fp8_f32 v133, v130, v131
	s_waitcnt vmcnt(17)
	v_mov_b32_e32 v130, v106
	s_waitcnt vmcnt(16)
	v_mov_b32_e32 v131, v110
	v_pk_mul_f32 v[130:131], v[130:131], s[72:73] op_sel_hi:[1,0]
	v_lshl_add_u32 v0, s21, 6, v140
	v_cvt_pk_fp8_f32 v133, v130, v131 op_sel:[0,0,1]
	v_mov_b32_e32 v130, v83
	v_mov_b32_e32 v131, v87
	v_pk_mul_f32 v[130:131], v[130:131], s[72:73] op_sel_hi:[1,0]
	s_nop 0
	v_cvt_pk_fp8_f32 v138, v130, v131
	v_mov_b32_e32 v130, v107
	v_mov_b32_e32 v131, v111
	v_pk_mul_f32 v[130:131], v[130:131], s[72:73] op_sel_hi:[1,0]
	s_nop 0
	v_cvt_pk_fp8_f32 v138, v130, v131 op_sel:[0,0,1]
	v_mov_b32_e32 v130, v84
	v_mov_b32_e32 v131, v88
	v_pk_mul_f32 v[130:131], v[130:131], s[72:73] op_sel_hi:[1,0]
	s_nop 0
	v_cvt_pk_fp8_f32 v139, v130, v131
	v_mov_b32_e32 v130, v108
	v_mov_b32_e32 v131, v112
	v_pk_mul_f32 v[130:131], v[130:131], s[72:73] op_sel_hi:[1,0]
	s_nop 0
	v_cvt_pk_fp8_f32 v139, v130, v131 op_sel:[0,0,1]
	v_mov_b32_e32 v130, v85
	v_mov_b32_e32 v131, v89
	v_pk_mul_f32 v[130:131], v[130:131], s[72:73] op_sel_hi:[1,0]
	s_nop 0
	v_cvt_pk_fp8_f32 v147, v130, v131
	v_mov_b32_e32 v130, v109
	v_mov_b32_e32 v131, v113
	v_pk_mul_f32 v[130:131], v[130:131], s[72:73] op_sel_hi:[1,0]
	s_nop 0
	v_cvt_pk_fp8_f32 v147, v130, v131 op_sel:[0,0,1]
	ds_write2_b32 v146, v133, v138 offset0:128 offset1:161
	ds_write2_b32 v146, v139, v147 offset0:194 offset1:227
	s_waitcnt lgkmcnt(0)
	s_barrier
	ds_read2_b32 v[130:131], v142 offset1:1
	ds_read2_b32 v[132:133], v142 offset0:2 offset1:3
	s_cbranch_scc1 .LBB0_537
	s_cmp_gt_i32 s40, 2
	s_cbranch_scc0 .LBB0_538
	s_cmp_eq_u32 s40, 3
	s_mov_b64 s[62:63], -1
	s_cbranch_scc0 .LBB0_535
	v_lshlrev_b32_e32 v138, 1, v0
	v_and_b32_e32 v139, 0x7f, v0
	s_movk_i32 s13, 0xff00
	v_and_or_b32 v138, v138, s13, v139
	s_mov_b64 s[62:63], 0

.LBB0_676:
	s_waitcnt vmcnt(20)

.Lcvw_a1:
	s_waitcnt vmcnt(0)
	s_branch .LBB0_531

.LBB0_975:
	s_waitcnt vmcnt(31)
	v_mov_b32_e32 v134, v2
	s_waitcnt vmcnt(30)
	v_mov_b32_e32 v135, v6
	v_pk_mul_f32 v[134:135], v[134:135], s[88:89] op_sel_hi:[1,0]
	v_mov_b32_e32 v136, v1
	v_cvt_pk_fp8_f32 v136, v134, v135
	s_waitcnt vmcnt(29)
	v_mov_b32_e32 v134, v10
	s_waitcnt vmcnt(28)
	v_mov_b32_e32 v135, v18
	v_pk_mul_f32 v[134:135], v[134:135], s[88:89] op_sel_hi:[1,0]
	v_mov_b32_e32 v137, v1
	v_cvt_pk_fp8_f32 v136, v134, v135 op_sel:[0,0,1]
	v_mov_b32_e32 v134, v3
	v_mov_b32_e32 v135, v7
	v_pk_mul_f32 v[134:135], v[134:135], s[88:89] op_sel_hi:[1,0]
	v_mov_b32_e32 v138, v1
	v_cvt_pk_fp8_f32 v137, v134, v135
	v_mov_b32_e32 v134, v11
	v_mov_b32_e32 v135, v19
	v_pk_mul_f32 v[134:135], v[134:135], s[88:89] op_sel_hi:[1,0]
	v_mov_b32_e32 v139, v1
	v_cvt_pk_fp8_f32 v137, v134, v135 op_sel:[0,0,1]
	v_mov_b32_e32 v134, v4
	v_mov_b32_e32 v135, v8
	v_pk_mul_f32 v[134:135], v[134:135], s[88:89] op_sel_hi:[1,0]
	v_mov_b32_e32 v144, v1
	v_cvt_pk_fp8_f32 v138, v134, v135
	v_mov_b32_e32 v134, v12
	v_mov_b32_e32 v135, v20
	v_pk_mul_f32 v[134:135], v[134:135], s[88:89] op_sel_hi:[1,0]
	v_mov_b32_e32 v145, v1
	v_cvt_pk_fp8_f32 v138, v134, v135 op_sel:[0,0,1]
	v_mov_b32_e32 v134, v5
	v_mov_b32_e32 v135, v9
	v_pk_mul_f32 v[134:135], v[134:135], s[88:89] op_sel_hi:[1,0]
	v_add_u32_e32 v152, 0x4000, v143
	v_cvt_pk_fp8_f32 v139, v134, v135
	v_mov_b32_e32 v134, v13
	v_mov_b32_e32 v135, v21
	v_pk_mul_f32 v[134:135], v[134:135], s[88:89] op_sel_hi:[1,0]
	v_add_u32_e32 v151, 0x8400, v143
	v_cvt_pk_fp8_f32 v139, v134, v135 op_sel:[0,0,1]
	s_waitcnt vmcnt(27)
	v_mov_b32_e32 v134, v22
	s_waitcnt vmcnt(26)
	v_mov_b32_e32 v135, v26
	ds_write2_b32 v143, v136, v137 offset1:33
	ds_write2_b32 v143, v138, v139 offset0:66 offset1:99
	v_pk_mul_f32 v[134:135], v[134:135], s[88:89] op_sel_hi:[1,0]
	v_mov_b32_e32 v136, v1
	v_cvt_pk_fp8_f32 v136, v134, v135
	s_waitcnt vmcnt(25)
	v_mov_b32_e32 v134, v30
	s_waitcnt vmcnt(24)
	v_mov_b32_e32 v135, v34
	v_pk_mul_f32 v[134:135], v[134:135], s[88:89] op_sel_hi:[1,0]
	v_mov_b32_e32 v137, v1
	v_cvt_pk_fp8_f32 v136, v134, v135 op_sel:[0,0,1]
	v_mov_b32_e32 v134, v23
	v_mov_b32_e32 v135, v27
	v_pk_mul_f32 v[134:135], v[134:135], s[88:89] op_sel_hi:[1,0]
	v_mov_b32_e32 v138, v1
	v_cvt_pk_fp8_f32 v137, v134, v135
	v_mov_b32_e32 v134, v31
	v_mov_b32_e32 v135, v35
	v_pk_mul_f32 v[134:135], v[134:135], s[88:89] op_sel_hi:[1,0]
	v_mov_b32_e32 v139, v1
	v_cvt_pk_fp8_f32 v137, v134, v135 op_sel:[0,0,1]
	v_mov_b32_e32 v134, v24
	v_mov_b32_e32 v135, v28
	v_pk_mul_f32 v[134:135], v[134:135], s[88:89] op_sel_hi:[1,0]
	v_mov_b32_e32 v146, v1
	v_cvt_pk_fp8_f32 v138, v134, v135
	v_mov_b32_e32 v134, v32
	v_mov_b32_e32 v135, v36
	v_pk_mul_f32 v[134:135], v[134:135], s[88:89] op_sel_hi:[1,0]
	s_cmp_lt_i32 s41, 2
	v_cvt_pk_fp8_f32 v138, v134, v135 op_sel:[0,0,1]
	v_mov_b32_e32 v134, v25
	v_mov_b32_e32 v135, v29
	v_pk_mul_f32 v[134:135], v[134:135], s[88:89] op_sel_hi:[1,0]
	s_nop 0
	v_cvt_pk_fp8_f32 v139, v134, v135
	v_mov_b32_e32 v134, v33
	v_mov_b32_e32 v135, v37
	v_pk_mul_f32 v[134:135], v[134:135], s[88:89] op_sel_hi:[1,0]
	s_nop 0
	v_cvt_pk_fp8_f32 v139, v134, v135 op_sel:[0,0,1]
	s_waitcnt vmcnt(23)
	v_mov_b32_e32 v134, v54
	s_waitcnt vmcnt(22)
	v_mov_b32_e32 v135, v58
	v_pk_mul_f32 v[134:135], v[134:135], s[88:89] op_sel_hi:[1,0]
	ds_write2_b32 v152, v136, v137 offset0:128 offset1:161
	ds_write2_b32 v152, v138, v139 offset0:194 offset1:227
	v_cvt_pk_fp8_f32 v144, v134, v135
	s_waitcnt vmcnt(21)
	v_mov_b32_e32 v134, v62
	s_waitcnt vmcnt(20)
	v_mov_b32_e32 v135, v66
	v_pk_mul_f32 v[134:135], v[134:135], s[88:89] op_sel_hi:[1,0]
	v_mov_b32_e32 v136, v1
	v_cvt_pk_fp8_f32 v144, v134, v135 op_sel:[0,0,1]
	v_mov_b32_e32 v134, v55
	v_mov_b32_e32 v135, v59
	v_pk_mul_f32 v[134:135], v[134:135], s[88:89] op_sel_hi:[1,0]
	v_mov_b32_e32 v137, v1
	v_cvt_pk_fp8_f32 v145, v134, v135
	v_mov_b32_e32 v134, v63
	v_mov_b32_e32 v135, v67
	v_pk_mul_f32 v[134:135], v[134:135], s[88:89] op_sel_hi:[1,0]
	v_mov_b32_e32 v138, v1
	v_cvt_pk_fp8_f32 v145, v134, v135 op_sel:[0,0,1]
	v_mov_b32_e32 v134, v56
	v_mov_b32_e32 v135, v60
	v_pk_mul_f32 v[134:135], v[134:135], s[88:89] op_sel_hi:[1,0]
	v_mov_b32_e32 v139, v1
	v_cvt_pk_fp8_f32 v136, v134, v135
	v_mov_b32_e32 v134, v64
	v_mov_b32_e32 v135, v68
	v_pk_mul_f32 v[134:135], v[134:135], s[88:89] op_sel_hi:[1,0]
	ds_write2_b32 v151, v144, v145 offset1:33
	v_cvt_pk_fp8_f32 v136, v134, v135 op_sel:[0,0,1]
	v_mov_b32_e32 v134, v57
	v_mov_b32_e32 v135, v61
	v_pk_mul_f32 v[134:135], v[134:135], s[88:89] op_sel_hi:[1,0]
	v_mov_b32_e32 v145, v1
	v_cvt_pk_fp8_f32 v137, v134, v135
	v_mov_b32_e32 v134, v65
	v_mov_b32_e32 v135, v69
	v_pk_mul_f32 v[134:135], v[134:135], s[88:89] op_sel_hi:[1,0]
	v_add_u32_e32 v144, 0xc400, v143
	v_cvt_pk_fp8_f32 v137, v134, v135 op_sel:[0,0,1]
	s_waitcnt vmcnt(19)
	v_mov_b32_e32 v134, v102
	s_waitcnt vmcnt(18)
	v_mov_b32_e32 v135, v106
	v_pk_mul_f32 v[134:135], v[134:135], s[88:89] op_sel_hi:[1,0]
	ds_write2_b32 v151, v136, v137 offset0:66 offset1:99
	v_cvt_pk_fp8_f32 v138, v134, v135
	s_waitcnt vmcnt(17)
	v_mov_b32_e32 v134, v110
	s_waitcnt vmcnt(16)
	v_mov_b32_e32 v135, v114
	v_pk_mul_f32 v[134:135], v[134:135], s[88:89] op_sel_hi:[1,0]
	s_nop 0
	v_cvt_pk_fp8_f32 v138, v134, v135 op_sel:[0,0,1]
	v_mov_b32_e32 v134, v103
	v_mov_b32_e32 v135, v107
	v_pk_mul_f32 v[134:135], v[134:135], s[88:89] op_sel_hi:[1,0]
	s_nop 0
	v_cvt_pk_fp8_f32 v139, v134, v135
	v_mov_b32_e32 v134, v111
	v_mov_b32_e32 v135, v115
	v_pk_mul_f32 v[134:135], v[134:135], s[88:89] op_sel_hi:[1,0]
	s_nop 0
	v_cvt_pk_fp8_f32 v139, v134, v135 op_sel:[0,0,1]
	v_mov_b32_e32 v134, v104
	v_mov_b32_e32 v135, v108
	v_pk_mul_f32 v[134:135], v[134:135], s[88:89] op_sel_hi:[1,0]
	s_nop 0
	v_cvt_pk_fp8_f32 v145, v134, v135
	v_mov_b32_e32 v134, v112
	v_mov_b32_e32 v135, v116
	v_pk_mul_f32 v[134:135], v[134:135], s[88:89] op_sel_hi:[1,0]
	s_nop 0
	v_cvt_pk_fp8_f32 v145, v134, v135 op_sel:[0,0,1]
	v_mov_b32_e32 v134, v105
	v_mov_b32_e32 v135, v109
	v_pk_mul_f32 v[134:135], v[134:135], s[88:89] op_sel_hi:[1,0]
	s_nop 0
	v_cvt_pk_fp8_f32 v146, v134, v135
	v_mov_b32_e32 v134, v113
	v_mov_b32_e32 v135, v117
	v_pk_mul_f32 v[134:135], v[134:135], s[88:89] op_sel_hi:[1,0]
	s_nop 0
	v_cvt_pk_fp8_f32 v146, v134, v135 op_sel:[0,0,1]
	ds_write2_b32 v144, v138, v139 offset0:128 offset1:161
	ds_write2_b32 v144, v145, v146 offset0:194 offset1:227
	s_waitcnt lgkmcnt(0)
	s_barrier
	ds_read2_b32 v[134:135], v142 offset1:1
	ds_read2_b32 v[136:137], v142 offset0:2 offset1:3
	v_lshl_add_u32 v139, s1, 6, v140
	s_cbranch_scc1 .LBB0_981
	s_cmp_gt_i32 s41, 2
	s_cbranch_scc0 .LBB0_982
	s_cmp_eq_u32 s41, 3
	s_mov_b64 s[52:53], -1
	s_cbranch_scc0 .LBB0_979
	v_lshlrev_b32_e32 v138, 1, v139
	v_and_b32_e32 v145, 0x7f, v139
	s_movk_i32 s15, 0xff00
	v_and_or_b32 v138, v138, s15, v145
	s_mov_b64 s[52:53], 0

.LBB0_2081:
	s_waitcnt vmcnt(31)
	v_mov_b32_e32 v128, v0
	s_waitcnt vmcnt(30)
	v_mov_b32_e32 v129, v4
	v_pk_mul_f32 v[128:129], v[128:129], s[34:35] op_sel_hi:[1,0]
	v_mov_b32_e32 v130, v135
	v_cvt_pk_fp8_f32 v130, v128, v129
	s_waitcnt vmcnt(29)
	v_mov_b32_e32 v128, v8
	s_waitcnt vmcnt(28)
	v_mov_b32_e32 v129, v12
	v_pk_mul_f32 v[128:129], v[128:129], s[34:35] op_sel_hi:[1,0]
	v_mov_b32_e32 v131, v135
	v_cvt_pk_fp8_f32 v130, v128, v129 op_sel:[0,0,1]
	v_mov_b32_e32 v128, v1
	v_mov_b32_e32 v129, v5
	v_pk_mul_f32 v[128:129], v[128:129], s[34:35] op_sel_hi:[1,0]
	v_mov_b32_e32 v134, v135
	v_cvt_pk_fp8_f32 v131, v128, v129
	v_mov_b32_e32 v128, v9
	v_mov_b32_e32 v129, v13
	v_pk_mul_f32 v[128:129], v[128:129], s[34:35] op_sel_hi:[1,0]
	v_mov_b32_e32 v138, v135
	v_cvt_pk_fp8_f32 v131, v128, v129 op_sel:[0,0,1]
	v_mov_b32_e32 v128, v2
	v_mov_b32_e32 v129, v6
	v_pk_mul_f32 v[128:129], v[128:129], s[34:35] op_sel_hi:[1,0]
	v_mov_b32_e32 v139, v135
	v_cvt_pk_fp8_f32 v134, v128, v129
	v_mov_b32_e32 v128, v10
	v_mov_b32_e32 v129, v14
	v_pk_mul_f32 v[128:129], v[128:129], s[34:35] op_sel_hi:[1,0]
	v_mov_b32_e32 v146, v135
	v_cvt_pk_fp8_f32 v134, v128, v129 op_sel:[0,0,1]
	v_mov_b32_e32 v128, v3
	v_mov_b32_e32 v129, v7
	v_pk_mul_f32 v[128:129], v[128:129], s[34:35] op_sel_hi:[1,0]
	v_add_u32_e32 v145, 0x4000, v143
	v_cvt_pk_fp8_f32 v138, v128, v129
	v_mov_b32_e32 v128, v11
	v_mov_b32_e32 v129, v15
	v_pk_mul_f32 v[128:129], v[128:129], s[34:35] op_sel_hi:[1,0]
	v_add_u32_e32 v144, 0x8400, v143
	v_cvt_pk_fp8_f32 v138, v128, v129 op_sel:[0,0,1]
	s_waitcnt vmcnt(27)
	v_mov_b32_e32 v128, v16
	s_waitcnt vmcnt(26)
	v_mov_b32_e32 v129, v20
	ds_write2_b32 v143, v130, v131 offset1:33
	ds_write2_b32 v143, v134, v138 offset0:66 offset1:99
	v_pk_mul_f32 v[128:129], v[128:129], s[34:35] op_sel_hi:[1,0]
	v_mov_b32_e32 v130, v135
	v_cvt_pk_fp8_f32 v130, v128, v129
	s_waitcnt vmcnt(25)
	v_mov_b32_e32 v128, v24
	s_waitcnt vmcnt(24)
	v_mov_b32_e32 v129, v28
	v_pk_mul_f32 v[128:129], v[128:129], s[34:35] op_sel_hi:[1,0]
	v_mov_b32_e32 v131, v135
	v_cvt_pk_fp8_f32 v130, v128, v129 op_sel:[0,0,1]
	v_mov_b32_e32 v128, v17
	v_mov_b32_e32 v129, v21
	v_pk_mul_f32 v[128:129], v[128:129], s[34:35] op_sel_hi:[1,0]
	v_mov_b32_e32 v134, v135
	v_cvt_pk_fp8_f32 v131, v128, v129
	v_mov_b32_e32 v128, v25
	v_mov_b32_e32 v129, v29
	v_pk_mul_f32 v[128:129], v[128:129], s[34:35] op_sel_hi:[1,0]
	v_mov_b32_e32 v138, v135
	v_cvt_pk_fp8_f32 v131, v128, v129 op_sel:[0,0,1]
	v_mov_b32_e32 v128, v18
	v_mov_b32_e32 v129, v22
	v_pk_mul_f32 v[128:129], v[128:129], s[34:35] op_sel_hi:[1,0]
	v_mov_b32_e32 v147, v135
	v_cvt_pk_fp8_f32 v134, v128, v129
	v_mov_b32_e32 v128, v26
	v_mov_b32_e32 v129, v30
	v_pk_mul_f32 v[128:129], v[128:129], s[34:35] op_sel_hi:[1,0]
	s_cmp_lt_i32 s78, 2
	v_cvt_pk_fp8_f32 v134, v128, v129 op_sel:[0,0,1]
	v_mov_b32_e32 v128, v19
	v_mov_b32_e32 v129, v23
	v_pk_mul_f32 v[128:129], v[128:129], s[34:35] op_sel_hi:[1,0]
	s_nop 0
	v_cvt_pk_fp8_f32 v138, v128, v129
	v_mov_b32_e32 v128, v27
	v_mov_b32_e32 v129, v31
	v_pk_mul_f32 v[128:129], v[128:129], s[34:35] op_sel_hi:[1,0]
	s_nop 0
	v_cvt_pk_fp8_f32 v138, v128, v129 op_sel:[0,0,1]
	s_waitcnt vmcnt(23)
	v_mov_b32_e32 v128, v48
	s_waitcnt vmcnt(22)
	v_mov_b32_e32 v129, v52
	v_pk_mul_f32 v[128:129], v[128:129], s[34:35] op_sel_hi:[1,0]
	ds_write2_b32 v145, v130, v131 offset0:128 offset1:161
	ds_write2_b32 v145, v134, v138 offset0:194 offset1:227
	v_cvt_pk_fp8_f32 v139, v128, v129
	s_waitcnt vmcnt(21)
	v_mov_b32_e32 v128, v56
	s_waitcnt vmcnt(20)
	v_mov_b32_e32 v129, v60
	v_pk_mul_f32 v[128:129], v[128:129], s[34:35] op_sel_hi:[1,0]
	v_mov_b32_e32 v130, v135
	v_cvt_pk_fp8_f32 v139, v128, v129 op_sel:[0,0,1]
	v_mov_b32_e32 v128, v49
	v_mov_b32_e32 v129, v53
	v_pk_mul_f32 v[128:129], v[128:129], s[34:35] op_sel_hi:[1,0]
	v_mov_b32_e32 v131, v135
	v_cvt_pk_fp8_f32 v146, v128, v129
	v_mov_b32_e32 v128, v57
	v_mov_b32_e32 v129, v61
	v_pk_mul_f32 v[128:129], v[128:129], s[34:35] op_sel_hi:[1,0]
	v_mov_b32_e32 v134, v135
	v_cvt_pk_fp8_f32 v146, v128, v129 op_sel:[0,0,1]
	v_mov_b32_e32 v128, v50
	v_mov_b32_e32 v129, v54
	v_pk_mul_f32 v[128:129], v[128:129], s[34:35] op_sel_hi:[1,0]
	v_mov_b32_e32 v138, v135
	v_cvt_pk_fp8_f32 v130, v128, v129
	v_mov_b32_e32 v128, v58
	v_mov_b32_e32 v129, v62
	v_pk_mul_f32 v[128:129], v[128:129], s[34:35] op_sel_hi:[1,0]
	ds_write2_b32 v144, v139, v146 offset1:33
	v_cvt_pk_fp8_f32 v130, v128, v129 op_sel:[0,0,1]
	v_mov_b32_e32 v128, v51
	v_mov_b32_e32 v129, v55
	v_pk_mul_f32 v[128:129], v[128:129], s[34:35] op_sel_hi:[1,0]
	v_mov_b32_e32 v139, v135
	v_cvt_pk_fp8_f32 v131, v128, v129
	v_mov_b32_e32 v128, v59
	v_mov_b32_e32 v129, v63
	v_pk_mul_f32 v[128:129], v[128:129], s[34:35] op_sel_hi:[1,0]
	v_add_u32_e32 v146, 0xc400, v143
	v_cvt_pk_fp8_f32 v131, v128, v129 op_sel:[0,0,1]
	s_waitcnt vmcnt(19)
	v_mov_b32_e32 v128, v96
	s_waitcnt vmcnt(18)
	v_mov_b32_e32 v129, v100
	v_pk_mul_f32 v[128:129], v[128:129], s[34:35] op_sel_hi:[1,0]
	ds_write2_b32 v144, v130, v131 offset0:66 offset1:99
	v_cvt_pk_fp8_f32 v134, v128, v129
	s_waitcnt vmcnt(17)
	v_mov_b32_e32 v128, v104
	s_waitcnt vmcnt(16)
	v_mov_b32_e32 v129, v108
	v_pk_mul_f32 v[128:129], v[128:129], s[34:35] op_sel_hi:[1,0]
	s_nop 0
	v_cvt_pk_fp8_f32 v134, v128, v129 op_sel:[0,0,1]
	v_mov_b32_e32 v128, v97
	v_mov_b32_e32 v129, v101
	v_pk_mul_f32 v[128:129], v[128:129], s[34:35] op_sel_hi:[1,0]
	s_nop 0
	v_cvt_pk_fp8_f32 v138, v128, v129
	v_mov_b32_e32 v128, v105
	v_mov_b32_e32 v129, v109
	v_pk_mul_f32 v[128:129], v[128:129], s[34:35] op_sel_hi:[1,0]
	s_nop 0
	v_cvt_pk_fp8_f32 v138, v128, v129 op_sel:[0,0,1]
	v_mov_b32_e32 v128, v98
	v_mov_b32_e32 v129, v102
	v_pk_mul_f32 v[128:129], v[128:129], s[34:35] op_sel_hi:[1,0]
	s_nop 0
	v_cvt_pk_fp8_f32 v139, v128, v129
	v_mov_b32_e32 v128, v106
	v_mov_b32_e32 v129, v110
	v_pk_mul_f32 v[128:129], v[128:129], s[34:35] op_sel_hi:[1,0]
	s_nop 0
	v_cvt_pk_fp8_f32 v139, v128, v129 op_sel:[0,0,1]
	v_mov_b32_e32 v128, v99
	v_mov_b32_e32 v129, v103
	v_pk_mul_f32 v[128:129], v[128:129], s[34:35] op_sel_hi:[1,0]
	s_nop 0
	v_cvt_pk_fp8_f32 v147, v128, v129
	v_mov_b32_e32 v128, v107
	v_mov_b32_e32 v129, v111
	v_pk_mul_f32 v[128:129], v[128:129], s[34:35] op_sel_hi:[1,0]
	s_nop 0
	v_cvt_pk_fp8_f32 v147, v128, v129 op_sel:[0,0,1]
	ds_write2_b32 v146, v134, v138 offset0:128 offset1:161
	ds_write2_b32 v146, v139, v147 offset0:194 offset1:227
	s_waitcnt lgkmcnt(0)
	s_barrier
	ds_read2_b32 v[128:129], v142 offset1:1
	ds_read2_b32 v[130:131], v142 offset0:2 offset1:3
	v_lshl_add_u32 v134, s77, 6, v140
	s_cbranch_scc1 .LBB0_2087
	s_cmp_gt_i32 s78, 2
	s_cbranch_scc0 .LBB0_2088
	s_cmp_eq_u32 s78, 3
	s_mov_b64 s[68:69], -1
	s_cbranch_scc0 .LBB0_2085
	v_lshlrev_b32_e32 v138, 1, v134
	v_and_b32_e32 v139, 0x7f, v134
	s_movk_i32 s11, 0xff00
	v_and_or_b32 v138, v138, s11, v139
	s_mov_b64 s[68:69], 0

.LBB0_4221:
	s_waitcnt vmcnt(31)
	v_mov_b32_e32 v128, v0
	s_waitcnt vmcnt(30)
	v_mov_b32_e32 v129, v4
	v_pk_mul_f32 v[128:129], v[128:129], s[68:69] op_sel_hi:[1,0]
	v_mov_b32_e32 v130, v171
	v_cvt_pk_fp8_f32 v130, v128, v129
	s_waitcnt vmcnt(29)
	v_mov_b32_e32 v128, v8
	s_waitcnt vmcnt(28)
	v_mov_b32_e32 v129, v12
	v_pk_mul_f32 v[128:129], v[128:129], s[68:69] op_sel_hi:[1,0]
	v_mov_b32_e32 v131, v171
	v_cvt_pk_fp8_f32 v130, v128, v129 op_sel:[0,0,1]
	v_mov_b32_e32 v128, v1
	v_mov_b32_e32 v129, v5
	v_pk_mul_f32 v[128:129], v[128:129], s[68:69] op_sel_hi:[1,0]
	v_mov_b32_e32 v136, v171
	v_cvt_pk_fp8_f32 v131, v128, v129
	v_mov_b32_e32 v128, v9
	v_mov_b32_e32 v129, v13
	v_pk_mul_f32 v[128:129], v[128:129], s[68:69] op_sel_hi:[1,0]
	v_mov_b32_e32 v137, v171
	v_cvt_pk_fp8_f32 v131, v128, v129 op_sel:[0,0,1]
	v_mov_b32_e32 v128, v2
	v_mov_b32_e32 v129, v6
	v_pk_mul_f32 v[128:129], v[128:129], s[68:69] op_sel_hi:[1,0]
	v_mov_b32_e32 v144, v171
	v_cvt_pk_fp8_f32 v136, v128, v129
	v_mov_b32_e32 v128, v10
	v_mov_b32_e32 v129, v14
	v_pk_mul_f32 v[128:129], v[128:129], s[68:69] op_sel_hi:[1,0]
	v_mov_b32_e32 v145, v171
	v_cvt_pk_fp8_f32 v136, v128, v129 op_sel:[0,0,1]
	v_mov_b32_e32 v128, v3
	v_mov_b32_e32 v129, v7
	v_pk_mul_f32 v[128:129], v[128:129], s[68:69] op_sel_hi:[1,0]
	v_add_u32_e32 v143, 0x4000, v141
	v_cvt_pk_fp8_f32 v137, v128, v129
	v_mov_b32_e32 v128, v11
	v_mov_b32_e32 v129, v15
	v_pk_mul_f32 v[128:129], v[128:129], s[68:69] op_sel_hi:[1,0]
	v_add_u32_e32 v142, 0x8400, v141
	v_cvt_pk_fp8_f32 v137, v128, v129 op_sel:[0,0,1]
	s_waitcnt vmcnt(27)
	v_mov_b32_e32 v128, v16
	s_waitcnt vmcnt(26)
	v_mov_b32_e32 v129, v20
	ds_write2_b32 v141, v130, v131 offset1:33
	ds_write2_b32 v141, v136, v137 offset0:66 offset1:99
	v_pk_mul_f32 v[128:129], v[128:129], s[68:69] op_sel_hi:[1,0]
	v_mov_b32_e32 v130, v171
	v_cvt_pk_fp8_f32 v130, v128, v129
	s_waitcnt vmcnt(25)
	v_mov_b32_e32 v128, v24
	s_waitcnt vmcnt(24)
	v_mov_b32_e32 v129, v28
	v_pk_mul_f32 v[128:129], v[128:129], s[68:69] op_sel_hi:[1,0]
	v_mov_b32_e32 v131, v171
	v_cvt_pk_fp8_f32 v130, v128, v129 op_sel:[0,0,1]
	v_mov_b32_e32 v128, v17
	v_mov_b32_e32 v129, v21
	v_pk_mul_f32 v[128:129], v[128:129], s[68:69] op_sel_hi:[1,0]
	v_mov_b32_e32 v136, v171
	v_cvt_pk_fp8_f32 v131, v128, v129
	v_mov_b32_e32 v128, v25
	v_mov_b32_e32 v129, v29
	v_pk_mul_f32 v[128:129], v[128:129], s[68:69] op_sel_hi:[1,0]
	v_mov_b32_e32 v137, v171
	v_cvt_pk_fp8_f32 v131, v128, v129 op_sel:[0,0,1]
	v_mov_b32_e32 v128, v18
	v_mov_b32_e32 v129, v22
	v_pk_mul_f32 v[128:129], v[128:129], s[68:69] op_sel_hi:[1,0]
	v_mov_b32_e32 v146, v171
	v_cvt_pk_fp8_f32 v136, v128, v129
	v_mov_b32_e32 v128, v26
	v_mov_b32_e32 v129, v30
	v_pk_mul_f32 v[128:129], v[128:129], s[68:69] op_sel_hi:[1,0]
	s_cmp_lt_i32 s66, 2
	v_cvt_pk_fp8_f32 v136, v128, v129 op_sel:[0,0,1]
	v_mov_b32_e32 v128, v19
	v_mov_b32_e32 v129, v23
	v_pk_mul_f32 v[128:129], v[128:129], s[68:69] op_sel_hi:[1,0]
	s_nop 0
	v_cvt_pk_fp8_f32 v137, v128, v129
	v_mov_b32_e32 v128, v27
	v_mov_b32_e32 v129, v31
	v_pk_mul_f32 v[128:129], v[128:129], s[68:69] op_sel_hi:[1,0]
	s_nop 0
	v_cvt_pk_fp8_f32 v137, v128, v129 op_sel:[0,0,1]
	s_waitcnt vmcnt(23)
	v_mov_b32_e32 v128, v48
	s_waitcnt vmcnt(22)
	v_mov_b32_e32 v129, v52
	v_pk_mul_f32 v[128:129], v[128:129], s[68:69] op_sel_hi:[1,0]
	ds_write2_b32 v143, v130, v131 offset0:128 offset1:161
	ds_write2_b32 v143, v136, v137 offset0:194 offset1:227
	v_cvt_pk_fp8_f32 v144, v128, v129
	s_waitcnt vmcnt(21)
	v_mov_b32_e32 v128, v56
	s_waitcnt vmcnt(20)
	v_mov_b32_e32 v129, v60
	v_pk_mul_f32 v[128:129], v[128:129], s[68:69] op_sel_hi:[1,0]
	v_mov_b32_e32 v130, v171
	v_cvt_pk_fp8_f32 v144, v128, v129 op_sel:[0,0,1]
	v_mov_b32_e32 v128, v49
	v_mov_b32_e32 v129, v53
	v_pk_mul_f32 v[128:129], v[128:129], s[68:69] op_sel_hi:[1,0]
	v_mov_b32_e32 v131, v171
	v_cvt_pk_fp8_f32 v145, v128, v129
	v_mov_b32_e32 v128, v57
	v_mov_b32_e32 v129, v61
	v_pk_mul_f32 v[128:129], v[128:129], s[68:69] op_sel_hi:[1,0]
	v_mov_b32_e32 v136, v171
	v_cvt_pk_fp8_f32 v145, v128, v129 op_sel:[0,0,1]
	v_mov_b32_e32 v128, v50
	v_mov_b32_e32 v129, v54
	v_pk_mul_f32 v[128:129], v[128:129], s[68:69] op_sel_hi:[1,0]
	v_mov_b32_e32 v137, v171
	v_cvt_pk_fp8_f32 v130, v128, v129
	v_mov_b32_e32 v128, v58
	v_mov_b32_e32 v129, v62
	v_pk_mul_f32 v[128:129], v[128:129], s[68:69] op_sel_hi:[1,0]
	ds_write2_b32 v142, v144, v145 offset1:33
	v_cvt_pk_fp8_f32 v130, v128, v129 op_sel:[0,0,1]
	v_mov_b32_e32 v128, v51
	v_mov_b32_e32 v129, v55
	v_pk_mul_f32 v[128:129], v[128:129], s[68:69] op_sel_hi:[1,0]
	v_mov_b32_e32 v145, v171
	v_cvt_pk_fp8_f32 v131, v128, v129
	v_mov_b32_e32 v128, v59
	v_mov_b32_e32 v129, v63
	v_pk_mul_f32 v[128:129], v[128:129], s[68:69] op_sel_hi:[1,0]
	v_add_u32_e32 v144, 0xc400, v141
	v_cvt_pk_fp8_f32 v131, v128, v129 op_sel:[0,0,1]
	s_waitcnt vmcnt(19)
	v_mov_b32_e32 v128, v96
	s_waitcnt vmcnt(18)
	v_mov_b32_e32 v129, v100
	v_pk_mul_f32 v[128:129], v[128:129], s[68:69] op_sel_hi:[1,0]
	ds_write2_b32 v142, v130, v131 offset0:66 offset1:99
	v_cvt_pk_fp8_f32 v136, v128, v129
	s_waitcnt vmcnt(17)
	v_mov_b32_e32 v128, v104
	s_waitcnt vmcnt(16)
	v_mov_b32_e32 v129, v108
	v_pk_mul_f32 v[128:129], v[128:129], s[68:69] op_sel_hi:[1,0]
	s_nop 0
	v_cvt_pk_fp8_f32 v136, v128, v129 op_sel:[0,0,1]
	v_mov_b32_e32 v128, v97
	v_mov_b32_e32 v129, v101
	v_pk_mul_f32 v[128:129], v[128:129], s[68:69] op_sel_hi:[1,0]
	s_nop 0
	v_cvt_pk_fp8_f32 v137, v128, v129
	v_mov_b32_e32 v128, v105
	v_mov_b32_e32 v129, v109
	v_pk_mul_f32 v[128:129], v[128:129], s[68:69] op_sel_hi:[1,0]
	s_nop 0
	v_cvt_pk_fp8_f32 v137, v128, v129 op_sel:[0,0,1]
	v_mov_b32_e32 v128, v98
	v_mov_b32_e32 v129, v102
	v_pk_mul_f32 v[128:129], v[128:129], s[68:69] op_sel_hi:[1,0]
	s_nop 0
	v_cvt_pk_fp8_f32 v145, v128, v129
	v_mov_b32_e32 v128, v106
	v_mov_b32_e32 v129, v110
	v_pk_mul_f32 v[128:129], v[128:129], s[68:69] op_sel_hi:[1,0]
	s_nop 0
	v_cvt_pk_fp8_f32 v145, v128, v129 op_sel:[0,0,1]
	v_mov_b32_e32 v128, v99
	v_mov_b32_e32 v129, v103
	v_pk_mul_f32 v[128:129], v[128:129], s[68:69] op_sel_hi:[1,0]
	s_nop 0
	v_cvt_pk_fp8_f32 v146, v128, v129
	v_mov_b32_e32 v128, v107
	v_mov_b32_e32 v129, v111
	v_pk_mul_f32 v[128:129], v[128:129], s[68:69] op_sel_hi:[1,0]
	s_nop 0
	v_cvt_pk_fp8_f32 v146, v128, v129 op_sel:[0,0,1]
	ds_write2_b32 v144, v136, v137 offset0:128 offset1:161
	ds_write2_b32 v144, v145, v146 offset0:194 offset1:227
	s_waitcnt lgkmcnt(0)
	s_barrier
	ds_read2_b32 v[128:129], v140 offset1:1
	ds_read2_b32 v[130:131], v140 offset0:2 offset1:3
	v_lshl_add_u32 v136, s65, 6, v138
	s_cbranch_scc1 .LBB0_4227
	s_cmp_gt_i32 s66, 2
	s_cbranch_scc0 .LBB0_4228
	s_cmp_eq_u32 s66, 3
	s_mov_b64 s[34:35], -1
	s_cbranch_scc0 .LBB0_4225
	v_lshlrev_b32_e32 v137, 1, v136
	v_and_b32_e32 v145, 0x7f, v136
	s_movk_i32 s11, 0xff00
	v_and_or_b32 v137, v137, s11, v145
	s_mov_b64 s[34:35], 0

.LBB0_4635:
	s_waitcnt vmcnt(31)
	v_mov_b32_e32 v130, v2
	s_waitcnt vmcnt(30)
	v_mov_b32_e32 v131, v6
	v_pk_mul_f32 v[130:131], v[130:131], s[64:65] op_sel_hi:[1,0]
	v_mov_b32_e32 v132, v1
	v_cvt_pk_fp8_f32 v132, v130, v131
	s_waitcnt vmcnt(29)
	v_mov_b32_e32 v130, v10
	s_waitcnt vmcnt(28)
	v_mov_b32_e32 v131, v14
	v_pk_mul_f32 v[130:131], v[130:131], s[64:65] op_sel_hi:[1,0]
	v_mov_b32_e32 v133, v1
	v_cvt_pk_fp8_f32 v132, v130, v131 op_sel:[0,0,1]
	v_mov_b32_e32 v130, v3
	v_mov_b32_e32 v131, v7
	v_pk_mul_f32 v[130:131], v[130:131], s[64:65] op_sel_hi:[1,0]
	v_mov_b32_e32 v136, v1
	v_cvt_pk_fp8_f32 v133, v130, v131
	v_mov_b32_e32 v130, v11
	v_mov_b32_e32 v131, v15
	v_pk_mul_f32 v[130:131], v[130:131], s[64:65] op_sel_hi:[1,0]
	v_mov_b32_e32 v137, v1
	v_cvt_pk_fp8_f32 v133, v130, v131 op_sel:[0,0,1]
	v_mov_b32_e32 v130, v4
	v_mov_b32_e32 v131, v8
	v_pk_mul_f32 v[130:131], v[130:131], s[64:65] op_sel_hi:[1,0]
	v_mov_b32_e32 v145, v1
	v_cvt_pk_fp8_f32 v136, v130, v131
	v_mov_b32_e32 v130, v12
	v_mov_b32_e32 v131, v16
	v_pk_mul_f32 v[130:131], v[130:131], s[64:65] op_sel_hi:[1,0]
	v_mov_b32_e32 v146, v1
	v_cvt_pk_fp8_f32 v136, v130, v131 op_sel:[0,0,1]
	v_mov_b32_e32 v130, v5
	v_mov_b32_e32 v131, v9
	v_pk_mul_f32 v[130:131], v[130:131], s[64:65] op_sel_hi:[1,0]
	v_add_u32_e32 v144, 0x4000, v142
	v_cvt_pk_fp8_f32 v137, v130, v131
	v_mov_b32_e32 v130, v13
	v_mov_b32_e32 v131, v17
	v_pk_mul_f32 v[130:131], v[130:131], s[64:65] op_sel_hi:[1,0]
	v_add_u32_e32 v143, 0x8400, v142
	v_cvt_pk_fp8_f32 v137, v130, v131 op_sel:[0,0,1]
	s_waitcnt vmcnt(27)
	v_mov_b32_e32 v130, v18
	s_waitcnt vmcnt(26)
	v_mov_b32_e32 v131, v22
	ds_write2_b32 v142, v132, v133 offset1:33
	ds_write2_b32 v142, v136, v137 offset0:66 offset1:99
	v_pk_mul_f32 v[130:131], v[130:131], s[64:65] op_sel_hi:[1,0]
	v_mov_b32_e32 v132, v1
	v_cvt_pk_fp8_f32 v132, v130, v131
	s_waitcnt vmcnt(25)
	v_mov_b32_e32 v130, v26
	s_waitcnt vmcnt(24)
	v_mov_b32_e32 v131, v30
	v_pk_mul_f32 v[130:131], v[130:131], s[64:65] op_sel_hi:[1,0]
	v_mov_b32_e32 v133, v1
	v_cvt_pk_fp8_f32 v132, v130, v131 op_sel:[0,0,1]
	v_mov_b32_e32 v130, v19
	v_mov_b32_e32 v131, v23
	v_pk_mul_f32 v[130:131], v[130:131], s[64:65] op_sel_hi:[1,0]
	v_mov_b32_e32 v136, v1
	v_cvt_pk_fp8_f32 v133, v130, v131
	v_mov_b32_e32 v130, v27
	v_mov_b32_e32 v131, v31
	v_pk_mul_f32 v[130:131], v[130:131], s[64:65] op_sel_hi:[1,0]
	v_mov_b32_e32 v137, v1
	v_cvt_pk_fp8_f32 v133, v130, v131 op_sel:[0,0,1]
	v_mov_b32_e32 v130, v20
	v_mov_b32_e32 v131, v24
	v_pk_mul_f32 v[130:131], v[130:131], s[64:65] op_sel_hi:[1,0]
	v_mov_b32_e32 v147, v1
	v_cvt_pk_fp8_f32 v136, v130, v131
	v_mov_b32_e32 v130, v28
	v_mov_b32_e32 v131, v32
	v_pk_mul_f32 v[130:131], v[130:131], s[64:65] op_sel_hi:[1,0]
	s_cmp_lt_i32 s66, 2
	v_cvt_pk_fp8_f32 v136, v130, v131 op_sel:[0,0,1]
	v_mov_b32_e32 v130, v21
	v_mov_b32_e32 v131, v25
	v_pk_mul_f32 v[130:131], v[130:131], s[64:65] op_sel_hi:[1,0]
	s_nop 0
	v_cvt_pk_fp8_f32 v137, v130, v131
	v_mov_b32_e32 v130, v29
	v_mov_b32_e32 v131, v33
	v_pk_mul_f32 v[130:131], v[130:131], s[64:65] op_sel_hi:[1,0]
	s_nop 0
	v_cvt_pk_fp8_f32 v137, v130, v131 op_sel:[0,0,1]
	s_waitcnt vmcnt(23)
	v_mov_b32_e32 v130, v50
	s_waitcnt vmcnt(22)
	v_mov_b32_e32 v131, v54
	v_pk_mul_f32 v[130:131], v[130:131], s[64:65] op_sel_hi:[1,0]
	ds_write2_b32 v144, v132, v133 offset0:128 offset1:161
	ds_write2_b32 v144, v136, v137 offset0:194 offset1:227
	v_cvt_pk_fp8_f32 v145, v130, v131
	s_waitcnt vmcnt(21)
	v_mov_b32_e32 v130, v74
	s_waitcnt vmcnt(20)
	v_mov_b32_e32 v131, v78
	v_pk_mul_f32 v[130:131], v[130:131], s[64:65] op_sel_hi:[1,0]
	v_mov_b32_e32 v132, v1
	v_cvt_pk_fp8_f32 v145, v130, v131 op_sel:[0,0,1]
	v_mov_b32_e32 v130, v51
	v_mov_b32_e32 v131, v55
	v_pk_mul_f32 v[130:131], v[130:131], s[64:65] op_sel_hi:[1,0]
	v_mov_b32_e32 v133, v1
	v_cvt_pk_fp8_f32 v146, v130, v131
	v_mov_b32_e32 v130, v75
	v_mov_b32_e32 v131, v79
	v_pk_mul_f32 v[130:131], v[130:131], s[64:65] op_sel_hi:[1,0]
	v_mov_b32_e32 v136, v1
	v_cvt_pk_fp8_f32 v146, v130, v131 op_sel:[0,0,1]
	v_mov_b32_e32 v130, v52
	v_mov_b32_e32 v131, v56
	v_pk_mul_f32 v[130:131], v[130:131], s[64:65] op_sel_hi:[1,0]
	v_mov_b32_e32 v137, v1
	v_cvt_pk_fp8_f32 v132, v130, v131
	v_mov_b32_e32 v130, v76
	v_mov_b32_e32 v131, v80
	v_pk_mul_f32 v[130:131], v[130:131], s[64:65] op_sel_hi:[1,0]
	ds_write2_b32 v143, v145, v146 offset1:33
	v_cvt_pk_fp8_f32 v132, v130, v131 op_sel:[0,0,1]
	v_mov_b32_e32 v130, v53
	v_mov_b32_e32 v131, v57
	v_pk_mul_f32 v[130:131], v[130:131], s[64:65] op_sel_hi:[1,0]
	v_mov_b32_e32 v146, v1
	v_cvt_pk_fp8_f32 v133, v130, v131
	v_mov_b32_e32 v130, v77
	v_mov_b32_e32 v131, v81
	v_pk_mul_f32 v[130:131], v[130:131], s[64:65] op_sel_hi:[1,0]
	v_add_u32_e32 v145, 0xc400, v142
	v_cvt_pk_fp8_f32 v133, v130, v131 op_sel:[0,0,1]
	s_waitcnt vmcnt(19)
	v_mov_b32_e32 v130, v98
	s_waitcnt vmcnt(18)
	v_mov_b32_e32 v131, v102
	v_pk_mul_f32 v[130:131], v[130:131], s[64:65] op_sel_hi:[1,0]
	ds_write2_b32 v143, v132, v133 offset0:66 offset1:99
	v_cvt_pk_fp8_f32 v136, v130, v131
	s_waitcnt vmcnt(17)
	v_mov_b32_e32 v130, v106
	s_waitcnt vmcnt(16)
	v_mov_b32_e32 v131, v110
	v_pk_mul_f32 v[130:131], v[130:131], s[64:65] op_sel_hi:[1,0]
	s_nop 0
	v_cvt_pk_fp8_f32 v136, v130, v131 op_sel:[0,0,1]
	v_mov_b32_e32 v130, v99
	v_mov_b32_e32 v131, v103
	v_pk_mul_f32 v[130:131], v[130:131], s[64:65] op_sel_hi:[1,0]
	s_nop 0
	v_cvt_pk_fp8_f32 v137, v130, v131
	v_mov_b32_e32 v130, v107
	v_mov_b32_e32 v131, v111
	v_pk_mul_f32 v[130:131], v[130:131], s[64:65] op_sel_hi:[1,0]
	s_nop 0
	v_cvt_pk_fp8_f32 v137, v130, v131 op_sel:[0,0,1]
	v_mov_b32_e32 v130, v100
	v_mov_b32_e32 v131, v104
	v_pk_mul_f32 v[130:131], v[130:131], s[64:65] op_sel_hi:[1,0]
	s_nop 0
	v_cvt_pk_fp8_f32 v146, v130, v131
	v_mov_b32_e32 v130, v108
	v_mov_b32_e32 v131, v112
	v_pk_mul_f32 v[130:131], v[130:131], s[64:65] op_sel_hi:[1,0]
	s_nop 0
	v_cvt_pk_fp8_f32 v146, v130, v131 op_sel:[0,0,1]
	v_mov_b32_e32 v130, v101
	v_mov_b32_e32 v131, v105
	v_pk_mul_f32 v[130:131], v[130:131], s[64:65] op_sel_hi:[1,0]
	s_nop 0
	v_cvt_pk_fp8_f32 v147, v130, v131
	v_mov_b32_e32 v130, v109
	v_mov_b32_e32 v131, v113
	v_pk_mul_f32 v[130:131], v[130:131], s[64:65] op_sel_hi:[1,0]
	s_nop 0
	v_cvt_pk_fp8_f32 v147, v130, v131 op_sel:[0,0,1]
	ds_write2_b32 v145, v136, v137 offset0:128 offset1:161
	ds_write2_b32 v145, v146, v147 offset0:194 offset1:227
	s_waitcnt lgkmcnt(0)
	s_barrier
	ds_read2_b32 v[130:131], v141 offset1:1
	ds_read2_b32 v[132:133], v141 offset0:2 offset1:3
	v_lshl_add_u32 v136, s67, 6, v139
	s_cbranch_scc1 .LBB0_4641
	s_cmp_gt_i32 s66, 2
	s_cbranch_scc0 .LBB0_4642
	s_cmp_eq_u32 s66, 3
	s_mov_b64 s[94:95], -1
	s_cbranch_scc0 .LBB0_4639
	v_lshlrev_b32_e32 v137, 1, v136
	v_and_b32_e32 v146, 0x7f, v136
	s_movk_i32 s19, 0xff00
	v_and_or_b32 v137, v137, s19, v146
	s_mov_b64 s[94:95], 0

.LBB0_5513:
	s_waitcnt vmcnt(31)
	v_mov_b32_e32 v128, v0
	s_waitcnt vmcnt(30)
	v_mov_b32_e32 v129, v4
	v_pk_mul_f32 v[128:129], v[128:129], s[40:41] op_sel_hi:[1,0]
	v_mov_b32_e32 v130, v135
	v_cvt_pk_fp8_f32 v130, v128, v129
	s_waitcnt vmcnt(29)
	v_mov_b32_e32 v128, v8
	s_waitcnt vmcnt(28)
	v_mov_b32_e32 v129, v12
	v_pk_mul_f32 v[128:129], v[128:129], s[40:41] op_sel_hi:[1,0]
	v_mov_b32_e32 v131, v135
	v_cvt_pk_fp8_f32 v130, v128, v129 op_sel:[0,0,1]
	v_mov_b32_e32 v128, v1
	v_mov_b32_e32 v129, v5
	v_pk_mul_f32 v[128:129], v[128:129], s[40:41] op_sel_hi:[1,0]
	v_mov_b32_e32 v134, v135
	v_cvt_pk_fp8_f32 v131, v128, v129
	v_mov_b32_e32 v128, v9
	v_mov_b32_e32 v129, v13
	v_pk_mul_f32 v[128:129], v[128:129], s[40:41] op_sel_hi:[1,0]
	v_mov_b32_e32 v138, v135
	v_cvt_pk_fp8_f32 v131, v128, v129 op_sel:[0,0,1]
	v_mov_b32_e32 v128, v2
	v_mov_b32_e32 v129, v6
	v_pk_mul_f32 v[128:129], v[128:129], s[40:41] op_sel_hi:[1,0]
	v_mov_b32_e32 v139, v135
	v_cvt_pk_fp8_f32 v134, v128, v129
	v_mov_b32_e32 v128, v10
	v_mov_b32_e32 v129, v14
	v_pk_mul_f32 v[128:129], v[128:129], s[40:41] op_sel_hi:[1,0]
	v_mov_b32_e32 v146, v135
	v_cvt_pk_fp8_f32 v134, v128, v129 op_sel:[0,0,1]
	v_mov_b32_e32 v128, v3
	v_mov_b32_e32 v129, v7
	v_pk_mul_f32 v[128:129], v[128:129], s[40:41] op_sel_hi:[1,0]
	v_add_u32_e32 v145, 0x4000, v143
	v_cvt_pk_fp8_f32 v138, v128, v129
	v_mov_b32_e32 v128, v11
	v_mov_b32_e32 v129, v15
	v_pk_mul_f32 v[128:129], v[128:129], s[40:41] op_sel_hi:[1,0]
	v_add_u32_e32 v144, 0x8400, v143
	v_cvt_pk_fp8_f32 v138, v128, v129 op_sel:[0,0,1]
	s_waitcnt vmcnt(27)
	v_mov_b32_e32 v128, v16
	s_waitcnt vmcnt(26)
	v_mov_b32_e32 v129, v20
	ds_write2_b32 v143, v130, v131 offset1:33
	ds_write2_b32 v143, v134, v138 offset0:66 offset1:99
	v_pk_mul_f32 v[128:129], v[128:129], s[40:41] op_sel_hi:[1,0]
	v_mov_b32_e32 v130, v135
	v_cvt_pk_fp8_f32 v130, v128, v129
	s_waitcnt vmcnt(25)
	v_mov_b32_e32 v128, v24
	s_waitcnt vmcnt(24)
	v_mov_b32_e32 v129, v28
	v_pk_mul_f32 v[128:129], v[128:129], s[40:41] op_sel_hi:[1,0]
	v_mov_b32_e32 v131, v135
	v_cvt_pk_fp8_f32 v130, v128, v129 op_sel:[0,0,1]
	v_mov_b32_e32 v128, v17
	v_mov_b32_e32 v129, v21
	v_pk_mul_f32 v[128:129], v[128:129], s[40:41] op_sel_hi:[1,0]
	v_mov_b32_e32 v134, v135
	v_cvt_pk_fp8_f32 v131, v128, v129
	v_mov_b32_e32 v128, v25
	v_mov_b32_e32 v129, v29
	v_pk_mul_f32 v[128:129], v[128:129], s[40:41] op_sel_hi:[1,0]
	v_mov_b32_e32 v138, v135
	v_cvt_pk_fp8_f32 v131, v128, v129 op_sel:[0,0,1]
	v_mov_b32_e32 v128, v18
	v_mov_b32_e32 v129, v22
	v_pk_mul_f32 v[128:129], v[128:129], s[40:41] op_sel_hi:[1,0]
	v_mov_b32_e32 v147, v135
	v_cvt_pk_fp8_f32 v134, v128, v129
	v_mov_b32_e32 v128, v26
	v_mov_b32_e32 v129, v30
	v_pk_mul_f32 v[128:129], v[128:129], s[40:41] op_sel_hi:[1,0]
	s_cmp_lt_i32 s73, 2
	v_cvt_pk_fp8_f32 v134, v128, v129 op_sel:[0,0,1]
	v_mov_b32_e32 v128, v19
	v_mov_b32_e32 v129, v23
	v_pk_mul_f32 v[128:129], v[128:129], s[40:41] op_sel_hi:[1,0]
	s_nop 0
	v_cvt_pk_fp8_f32 v138, v128, v129
	v_mov_b32_e32 v128, v27
	v_mov_b32_e32 v129, v31
	v_pk_mul_f32 v[128:129], v[128:129], s[40:41] op_sel_hi:[1,0]
	s_nop 0
	v_cvt_pk_fp8_f32 v138, v128, v129 op_sel:[0,0,1]
	s_waitcnt vmcnt(23)
	v_mov_b32_e32 v128, v48
	s_waitcnt vmcnt(22)
	v_mov_b32_e32 v129, v52
	v_pk_mul_f32 v[128:129], v[128:129], s[40:41] op_sel_hi:[1,0]
	ds_write2_b32 v145, v130, v131 offset0:128 offset1:161
	ds_write2_b32 v145, v134, v138 offset0:194 offset1:227
	v_cvt_pk_fp8_f32 v139, v128, v129
	s_waitcnt vmcnt(21)
	v_mov_b32_e32 v128, v56
	s_waitcnt vmcnt(20)
	v_mov_b32_e32 v129, v60
	v_pk_mul_f32 v[128:129], v[128:129], s[40:41] op_sel_hi:[1,0]
	v_mov_b32_e32 v130, v135
	v_cvt_pk_fp8_f32 v139, v128, v129 op_sel:[0,0,1]
	v_mov_b32_e32 v128, v49
	v_mov_b32_e32 v129, v53
	v_pk_mul_f32 v[128:129], v[128:129], s[40:41] op_sel_hi:[1,0]
	v_mov_b32_e32 v131, v135
	v_cvt_pk_fp8_f32 v146, v128, v129
	v_mov_b32_e32 v128, v57
	v_mov_b32_e32 v129, v61
	v_pk_mul_f32 v[128:129], v[128:129], s[40:41] op_sel_hi:[1,0]
	v_mov_b32_e32 v134, v135
	v_cvt_pk_fp8_f32 v146, v128, v129 op_sel:[0,0,1]
	v_mov_b32_e32 v128, v50
	v_mov_b32_e32 v129, v54
	v_pk_mul_f32 v[128:129], v[128:129], s[40:41] op_sel_hi:[1,0]
	v_mov_b32_e32 v138, v135
	v_cvt_pk_fp8_f32 v130, v128, v129
	v_mov_b32_e32 v128, v58
	v_mov_b32_e32 v129, v62
	v_pk_mul_f32 v[128:129], v[128:129], s[40:41] op_sel_hi:[1,0]
	ds_write2_b32 v144, v139, v146 offset1:33
	v_cvt_pk_fp8_f32 v130, v128, v129 op_sel:[0,0,1]
	v_mov_b32_e32 v128, v51
	v_mov_b32_e32 v129, v55
	v_pk_mul_f32 v[128:129], v[128:129], s[40:41] op_sel_hi:[1,0]
	v_mov_b32_e32 v139, v135
	v_cvt_pk_fp8_f32 v131, v128, v129
	v_mov_b32_e32 v128, v59
	v_mov_b32_e32 v129, v63
	v_pk_mul_f32 v[128:129], v[128:129], s[40:41] op_sel_hi:[1,0]
	v_add_u32_e32 v146, 0xc400, v143
	v_cvt_pk_fp8_f32 v131, v128, v129 op_sel:[0,0,1]
	s_waitcnt vmcnt(19)
	v_mov_b32_e32 v128, v96
	s_waitcnt vmcnt(18)
	v_mov_b32_e32 v129, v100
	v_pk_mul_f32 v[128:129], v[128:129], s[40:41] op_sel_hi:[1,0]
	ds_write2_b32 v144, v130, v131 offset0:66 offset1:99
	v_cvt_pk_fp8_f32 v134, v128, v129
	s_waitcnt vmcnt(17)
	v_mov_b32_e32 v128, v104
	s_waitcnt vmcnt(16)
	v_mov_b32_e32 v129, v108
	v_pk_mul_f32 v[128:129], v[128:129], s[40:41] op_sel_hi:[1,0]
	s_nop 0
	v_cvt_pk_fp8_f32 v134, v128, v129 op_sel:[0,0,1]
	v_mov_b32_e32 v128, v97
	v_mov_b32_e32 v129, v101
	v_pk_mul_f32 v[128:129], v[128:129], s[40:41] op_sel_hi:[1,0]
	s_nop 0
	v_cvt_pk_fp8_f32 v138, v128, v129
	v_mov_b32_e32 v128, v105
	v_mov_b32_e32 v129, v109
	v_pk_mul_f32 v[128:129], v[128:129], s[40:41] op_sel_hi:[1,0]
	s_nop 0
	v_cvt_pk_fp8_f32 v138, v128, v129 op_sel:[0,0,1]
	v_mov_b32_e32 v128, v98
	v_mov_b32_e32 v129, v102
	v_pk_mul_f32 v[128:129], v[128:129], s[40:41] op_sel_hi:[1,0]
	s_nop 0
	v_cvt_pk_fp8_f32 v139, v128, v129
	v_mov_b32_e32 v128, v106
	v_mov_b32_e32 v129, v110
	v_pk_mul_f32 v[128:129], v[128:129], s[40:41] op_sel_hi:[1,0]
	s_nop 0
	v_cvt_pk_fp8_f32 v139, v128, v129 op_sel:[0,0,1]
	v_mov_b32_e32 v128, v99
	v_mov_b32_e32 v129, v103
	v_pk_mul_f32 v[128:129], v[128:129], s[40:41] op_sel_hi:[1,0]
	s_nop 0
	v_cvt_pk_fp8_f32 v147, v128, v129
	v_mov_b32_e32 v128, v107
	v_mov_b32_e32 v129, v111
	v_pk_mul_f32 v[128:129], v[128:129], s[40:41] op_sel_hi:[1,0]
	s_nop 0
	v_cvt_pk_fp8_f32 v147, v128, v129 op_sel:[0,0,1]
	ds_write2_b32 v146, v134, v138 offset0:128 offset1:161
	ds_write2_b32 v146, v139, v147 offset0:194 offset1:227
	s_waitcnt lgkmcnt(0)
	s_barrier
	ds_read2_b32 v[128:129], v142 offset1:1
	ds_read2_b32 v[130:131], v142 offset0:2 offset1:3
	v_lshl_add_u32 v134, s72, 6, v140
	s_cbranch_scc1 .LBB0_5519
	s_cmp_gt_i32 s73, 2
	s_cbranch_scc0 .LBB0_5520
	s_cmp_eq_u32 s73, 3
	s_mov_b64 s[68:69], -1
	s_cbranch_scc0 .LBB0_5517
	v_lshlrev_b32_e32 v138, 1, v134
	v_and_b32_e32 v139, 0x7f, v134
	s_movk_i32 s19, 0xff00
	v_and_or_b32 v138, v138, s19, v139
	s_mov_b64 s[68:69], 0
